# v40 + early L2 write-back only by the workgroup that arrives with 16 peers outstanding at its XCD barrier counter
# baseline (speedup 1.0000x reference)
.LBB0_241:
	s_lshl_b32 s18, s33, 6
	s_add_i32 s92, s18, 0x500
	s_lshl_b64 s[0:1], s[92:93], 2
	v_lshl_add_u64 v[8:9], v[4:5], 0, s[0:1]
	v_mov_b32_e32 v1, 1
	flat_atomic_add v1, v[8:9], v1 sc0
	v_cvt_f32_u32_e32 v7, v6
	v_sub_u32_e32 v8, 0, v6
	v_rcp_iflag_f32_e32 v7, v7
	s_nop 0
	v_mul_f32_e32 v7, 0x4f7ffffe, v7
	v_cvt_u32_f32_e32 v7, v7
	v_mul_lo_u32 v8, v8, v7
	v_mul_hi_u32 v8, v7, v8
	v_add_u32_e32 v7, v7, v8
	s_waitcnt vmcnt(0) lgkmcnt(0)
	v_mul_hi_u32 v7, v1, v7
	v_mul_lo_u32 v9, v7, v6
	v_add_u32_e32 v8, 1, v1
	v_sub_u32_e32 v1, v1, v9
	v_add_u32_e32 v10, 1, v7
	v_cmp_ge_u32_e32 vcc, v1, v6
	v_sub_u32_e32 v9, v1, v6
	s_nop 0
	v_cndmask_b32_e32 v7, v7, v10, vcc
	v_cndmask_b32_e32 v1, v1, v9, vcc
	v_add_u32_e32 v9, 1, v7
	v_cmp_ge_u32_e32 vcc, v1, v6
	s_nop 1
	v_cndmask_b32_e32 v1, v7, v9, vcc
	v_mad_u64_u32 v[6:7], s[0:1], v6, v1, v[6:7]
	v_cmp_ne_u32_e32 vcc, v8, v6
	s_and_saveexec_b64 s[0:1], vcc
	s_xor_b64 s[0:1], exec, s[0:1]
	s_cbranch_execz .LBB0_254
	v_sub_u32_e32 v2, v6, v8
	v_lshlrev_b32_e64 v2, v2, 1
	v_and_b32_e32 v2, 0x10000, v2
	v_cmp_ne_u32_e32 vcc, 0, v2
	s_cbranch_vccz .Lewb_1
	buffer_wbl2 sc1

.LBB0_483:
	s_lshl_b32 s18, s34, 6
	s_add_i32 s92, s18, 0x500
	s_lshl_b64 s[0:1], s[92:93], 2
	v_lshl_add_u64 v[8:9], v[4:5], 0, s[0:1]
	v_mov_b32_e32 v1, 1
	flat_atomic_add v7, v[8:9], v1 sc0
	v_cvt_f32_u32_e32 v1, v6
	v_sub_u32_e32 v8, 0, v6
	v_rcp_iflag_f32_e32 v1, v1
	s_nop 0
	v_mul_f32_e32 v1, 0x4f7ffffe, v1
	v_cvt_u32_f32_e32 v1, v1
	v_mul_lo_u32 v8, v8, v1
	v_mul_hi_u32 v8, v1, v8
	v_add_u32_e32 v1, v1, v8
	s_waitcnt vmcnt(0) lgkmcnt(0)
	v_mul_hi_u32 v1, v7, v1
	v_mul_lo_u32 v8, v1, v6
	v_sub_u32_e32 v8, v7, v8
	v_cmp_ge_u32_e32 vcc, v8, v6
	v_add_u32_e32 v9, 1, v1
	s_nop 0
	v_cndmask_b32_e32 v1, v1, v9, vcc
	v_sub_u32_e32 v9, v8, v6
	v_cndmask_b32_e32 v8, v8, v9, vcc
	v_cmp_ge_u32_e32 vcc, v8, v6
	v_add_u32_e32 v8, 1, v1
	s_nop 0
	v_cndmask_b32_e32 v1, v1, v8, vcc
	v_add_u32_e32 v8, 1, v7
	v_mad_u64_u32 v[6:7], s[0:1], v6, v1, v[6:7]
	v_cmp_ne_u32_e32 vcc, v8, v6
	s_and_saveexec_b64 s[0:1], vcc
	s_xor_b64 s[0:1], exec, s[0:1]
	s_cbranch_execz .LBB0_496
	v_sub_u32_e32 v2, v6, v8
	v_lshlrev_b32_e64 v2, v2, 1
	v_and_b32_e32 v2, 0x10000, v2
	v_cmp_ne_u32_e32 vcc, 0, v2
	s_cbranch_vccz .Lewb_2
	buffer_wbl2 sc1

.LBB0_1095:
	s_lshl_b32 s20, s33, 6
	s_add_i32 s92, s20, 0x500
	s_lshl_b64 s[0:1], s[92:93], 2
	v_lshl_add_u64 v[8:9], v[4:5], 0, s[0:1]
	v_mov_b32_e32 v1, 1
	flat_atomic_add v7, v[8:9], v1 sc0
	v_cvt_f32_u32_e32 v1, v6
	v_sub_u32_e32 v8, 0, v6
	v_rcp_iflag_f32_e32 v1, v1
	s_nop 0
	v_mul_f32_e32 v1, 0x4f7ffffe, v1
	v_cvt_u32_f32_e32 v1, v1
	v_mul_lo_u32 v8, v8, v1
	v_mul_hi_u32 v8, v1, v8
	v_add_u32_e32 v1, v1, v8
	s_waitcnt vmcnt(0) lgkmcnt(0)
	v_mul_hi_u32 v1, v7, v1
	v_mul_lo_u32 v8, v1, v6
	v_sub_u32_e32 v8, v7, v8
	v_cmp_ge_u32_e32 vcc, v8, v6
	v_add_u32_e32 v9, 1, v1
	s_nop 0
	v_cndmask_b32_e32 v1, v1, v9, vcc
	v_sub_u32_e32 v9, v8, v6
	v_cndmask_b32_e32 v8, v8, v9, vcc
	v_cmp_ge_u32_e32 vcc, v8, v6
	v_add_u32_e32 v8, 1, v1
	s_nop 0
	v_cndmask_b32_e32 v1, v1, v8, vcc
	v_add_u32_e32 v8, 1, v7
	v_mad_u64_u32 v[6:7], s[0:1], v6, v1, v[6:7]
	v_cmp_ne_u32_e32 vcc, v8, v6
	s_and_saveexec_b64 s[0:1], vcc
	s_xor_b64 s[0:1], exec, s[0:1]
	s_cbranch_execz .LBB0_1108
	v_sub_u32_e32 v2, v6, v8
	v_lshlrev_b32_e64 v2, v2, 1
	v_and_b32_e32 v2, 0x10000, v2
	v_cmp_ne_u32_e32 vcc, 0, v2
	s_cbranch_vccz .Lewb_6
	buffer_wbl2 sc1

.LBB0_1358:
	s_lshl_b32 s18, s33, 6
	s_add_i32 s92, s18, 0x500
	s_lshl_b64 s[0:1], s[92:93], 2
	v_lshl_add_u64 v[8:9], v[4:5], 0, s[0:1]
	v_mov_b32_e32 v1, 1
	flat_atomic_add v7, v[8:9], v1 sc0
	v_cvt_f32_u32_e32 v1, v6
	v_sub_u32_e32 v8, 0, v6
	v_rcp_iflag_f32_e32 v1, v1
	s_nop 0
	v_mul_f32_e32 v1, 0x4f7ffffe, v1
	v_cvt_u32_f32_e32 v1, v1
	v_mul_lo_u32 v8, v8, v1
	v_mul_hi_u32 v8, v1, v8
	v_add_u32_e32 v1, v1, v8
	s_waitcnt vmcnt(0) lgkmcnt(0)
	v_mul_hi_u32 v1, v7, v1
	v_mul_lo_u32 v8, v1, v6
	v_sub_u32_e32 v8, v7, v8
	v_cmp_ge_u32_e32 vcc, v8, v6
	v_add_u32_e32 v9, 1, v1
	s_nop 0
	v_cndmask_b32_e32 v1, v1, v9, vcc
	v_sub_u32_e32 v9, v8, v6
	v_cndmask_b32_e32 v8, v8, v9, vcc
	v_cmp_ge_u32_e32 vcc, v8, v6
	v_add_u32_e32 v8, 1, v1
	s_nop 0
	v_cndmask_b32_e32 v1, v1, v8, vcc
	v_add_u32_e32 v8, 1, v7
	v_mad_u64_u32 v[6:7], s[0:1], v6, v1, v[6:7]
	v_cmp_ne_u32_e32 vcc, v8, v6
	s_and_saveexec_b64 s[0:1], vcc
	s_xor_b64 s[0:1], exec, s[0:1]
	s_cbranch_execz .LBB0_1371
	v_sub_u32_e32 v2, v6, v8
	v_lshlrev_b32_e64 v2, v2, 1
	v_and_b32_e32 v2, 0x10000, v2
	v_cmp_ne_u32_e32 vcc, 0, v2
	s_cbranch_vccz .Lewb_8
	buffer_wbl2 sc1

.LBB0_1738:
	s_lshl_b32 s18, s33, 6
	s_add_i32 s92, s18, 0x500
	s_lshl_b64 s[0:1], s[92:93], 2
	v_lshl_add_u64 v[8:9], v[4:5], 0, s[0:1]
	v_mov_b32_e32 v1, 1
	flat_atomic_add v7, v[8:9], v1 sc0
	v_cvt_f32_u32_e32 v1, v6
	v_sub_u32_e32 v8, 0, v6
	v_rcp_iflag_f32_e32 v1, v1
	s_nop 0
	v_mul_f32_e32 v1, 0x4f7ffffe, v1
	v_cvt_u32_f32_e32 v1, v1
	v_mul_lo_u32 v8, v8, v1
	v_mul_hi_u32 v8, v1, v8
	v_add_u32_e32 v1, v1, v8
	s_waitcnt vmcnt(0) lgkmcnt(0)
	v_mul_hi_u32 v1, v7, v1
	v_mul_lo_u32 v8, v1, v6
	v_sub_u32_e32 v8, v7, v8
	v_cmp_ge_u32_e32 vcc, v8, v6
	v_add_u32_e32 v9, 1, v1
	s_nop 0
	v_cndmask_b32_e32 v1, v1, v9, vcc
	v_sub_u32_e32 v9, v8, v6
	v_cndmask_b32_e32 v8, v8, v9, vcc
	v_cmp_ge_u32_e32 vcc, v8, v6
	v_add_u32_e32 v8, 1, v1
	s_nop 0
	v_cndmask_b32_e32 v1, v1, v8, vcc
	v_add_u32_e32 v8, 1, v7
	v_mad_u64_u32 v[6:7], s[0:1], v6, v1, v[6:7]
	v_cmp_ne_u32_e32 vcc, v8, v6
	s_and_saveexec_b64 s[0:1], vcc
	s_xor_b64 s[0:1], exec, s[0:1]
	v_readlane_b32 s26, v255, 25
	s_cbranch_execz .LBB0_1751
	v_sub_u32_e32 v2, v6, v8
	v_lshlrev_b32_e64 v2, v2, 1
	v_and_b32_e32 v2, 0x10000, v2
	v_cmp_ne_u32_e32 vcc, 0, v2
	s_cbranch_vccz .Lewb_11
	buffer_wbl2 sc1
